# speedup vs baseline: 1.0210x; 1.0210x over previous
_Z7k_stageILi0ELi8EEv8AttnArgsPKDF16_PKfPDF16_iii:
	s_load_dwordx16 s[64:79], s[0:1], 0x40
	s_load_dwordx16 s[64:79], s[0:1], 0x0
	v_readfirstlane_b32 s94, v0
	s_nop 0
	s_lshr_b32 s94, s94, 6
	s_cmp_lt_u32 s94, 4
	s_cbranch_scc1 .Lmyprio3
	s_setprio 1

.LBB3_82:
	s_setprio 0
	s_mul_i32 s0, s9, s3
	s_lshl_b32 s1, s30, 6
	s_add_i32 s0, s0, s8
	s_or_b32 s1, s1, s31
	s_or_b32 s7, s1, s11
	s_mul_i32 s4, s0, 0x60000
	s_mul_hi_i32 s1, s0, 0x60000
	s_waitcnt lgkmcnt(0)
	s_add_u32 s6, s12, s4
	s_mulk_i32 s0, 0x300
	s_addc_u32 s8, s13, s1
	s_ashr_i32 s1, s0, 31
	s_lshl_b64 s[0:1], s[0:1], 2
	s_add_u32 s4, s14, s0
	s_addc_u32 s5, s15, s1
	s_mul_i32 s0, s2, 0x1800000
	s_mul_hi_u32 s1, s3, 0x1800000
	s_add_i32 s1, s1, s0
	s_mul_i32 s0, s3, 0x1800000
	s_add_u32 s0, s20, s0
	v_readfirstlane_b32 s2, v0
	s_addc_u32 s1, s21, s1
	s_lshr_b32 s9, s2, 6
	s_and_b32 s1, s1, 0xffff
	s_mul_i32 s2, s9, 0x6000
	v_and_b32_e32 v2, 63, v0
	s_mul_hi_u32 s3, s9, 0x6000
	s_add_u32 s2, s6, s2
	s_addc_u32 s3, s8, s3
	v_lshlrev_b32_e32 v82, 4, v2
	v_mov_b32_e32 v83, 0
	v_lshl_add_u64 v[118:119], s[2:3], 0, v[82:83]
	s_movk_i32 s6, 0x1000
	v_add_co_u32_e32 v50, vcc, s6, v118
	s_movk_i32 s6, 0x2000
	s_nop 0
	v_addc_co_u32_e32 v51, vcc, 0, v119, vcc
	v_add_co_u32_e32 v52, vcc, s6, v118
	global_load_dwordx4 v[2:5], v82, s[2:3] offset:1024
	global_load_dwordx4 v[6:9], v82, s[2:3] offset:2048
	v_addc_co_u32_e32 v53, vcc, 0, v119, vcc
	global_load_dwordx4 v[10:13], v82, s[2:3] offset:3072
	global_load_dwordx4 v[14:17], v[52:53], off offset:-4096
	global_load_dwordx4 v[18:21], v[50:51], off offset:1024
	global_load_dwordx4 v[22:25], v[50:51], off offset:2048
	global_load_dwordx4 v[26:29], v82, s[2:3]
	global_load_dwordx4 v[30:33], v[50:51], off offset:3072
	global_load_dwordx4 v[34:37], v[52:53], off
	global_load_dwordx4 v[38:41], v[52:53], off offset:1024
	global_load_dwordx4 v[42:45], v[52:53], off offset:2048
	global_load_dwordx4 v[46:49], v[52:53], off offset:3072
	s_movk_i32 s2, 0x3000
	v_add_co_u32_e32 v116, vcc, s2, v118
	s_movk_i32 s2, 0x4000
	s_nop 0
	v_addc_co_u32_e32 v117, vcc, 0, v119, vcc
	v_add_co_u32_e32 v156, vcc, s2, v118
	s_nop 1
	v_addc_co_u32_e32 v157, vcc, 0, v119, vcc
	s_barrier
	s_cmp_lt_u32 s94, 4
	s_cbranch_scc1 .Lmystag3_1
	s_sleep 7

_Z7k_stageILi1ELi4EEv8AttnArgsPKDF16_PKfPDF16_iii:
	s_load_dwordx16 s[64:79], s[0:1], 0x0
	v_readfirstlane_b32 s94, v0
	s_nop 0
	s_lshr_b32 s94, s94, 6
	s_cmp_lt_u32 s94, 4
	s_cbranch_scc1 .Lmyprio4
	s_setprio 1

.LBB4_155:
	s_setprio 0
	s_load_dword s0, s[0:1], 0x88
	s_lshl_b32 s1, s45, 6
	s_and_b32 s1, s1, 0xfffffe00
	s_or_b32 s2, s1, s44
	v_readfirstlane_b32 s4, v0
	s_waitcnt lgkmcnt(0)
	s_mul_i32 s3, s0, 0x60000
	s_mul_hi_i32 s1, s0, 0x60000
	s_add_u32 s3, s28, s3
	s_mulk_i32 s0, 0x300
	s_addc_u32 s5, s29, s1
	s_ashr_i32 s1, s0, 31
	s_lshl_b64 s[0:1], s[0:1], 2
	s_add_u32 s0, s30, s0
	s_addc_u32 s1, s31, s1
	s_lshr_b32 s6, s4, 6
	s_and_b32 s25, s25, 0xffff
	s_mul_i32 s4, s6, 0x6000
	v_and_b32_e32 v2, 63, v0
	s_mul_hi_u32 s7, s6, 0x6000
	s_add_u32 s4, s3, s4
	s_addc_u32 s5, s5, s7
	v_lshlrev_b32_e32 v56, 4, v2
	v_mov_b32_e32 v57, 0
	v_lshl_add_u64 v[54:55], s[4:5], 0, v[56:57]
	s_movk_i32 s3, 0x1000
	v_add_co_u32_e32 v50, vcc, s3, v54
	s_movk_i32 s3, 0x2000
	s_nop 0
	v_addc_co_u32_e32 v51, vcc, 0, v55, vcc
	v_add_co_u32_e32 v52, vcc, s3, v54
	global_load_dwordx4 v[2:5], v56, s[4:5] offset:1024
	global_load_dwordx4 v[6:9], v56, s[4:5] offset:2048
	v_addc_co_u32_e32 v53, vcc, 0, v55, vcc
	global_load_dwordx4 v[10:13], v56, s[4:5] offset:3072
	global_load_dwordx4 v[14:17], v[52:53], off offset:-4096
	global_load_dwordx4 v[18:21], v[50:51], off offset:1024
	global_load_dwordx4 v[22:25], v[50:51], off offset:2048
	global_load_dwordx4 v[26:29], v56, s[4:5]
	global_load_dwordx4 v[30:33], v[50:51], off offset:3072
	global_load_dwordx4 v[34:37], v[52:53], off
	global_load_dwordx4 v[38:41], v[52:53], off offset:1024
	global_load_dwordx4 v[42:45], v[52:53], off offset:2048
	global_load_dwordx4 v[46:49], v[52:53], off offset:3072
	s_movk_i32 s3, 0x3000
	v_add_co_u32_e32 v58, vcc, s3, v54
	s_movk_i32 s3, 0x4000
	s_nop 0
	v_addc_co_u32_e32 v59, vcc, 0, v55, vcc
	v_add_co_u32_e32 v140, vcc, s3, v54
	s_nop 1
	v_addc_co_u32_e32 v141, vcc, 0, v55, vcc
	s_barrier
	s_cmp_lt_u32 s94, 4
	s_cbranch_scc1 .Lmystag4_1
	s_sleep 4
